# grid barrier wake-up flattened: last XCD leader releases all per-XCC generation words itself, removing one atomic+poll hop per barrier
# speedup vs baseline: 1.0084x; 1.0034x over previous
.LBB0_159:
	s_or_b64 exec, exec, s[6:7]
	s_and_saveexec_b64 s[6:7], s[10:11]
	s_cbranch_execz .LBB0_161
	v_mov_b32_e32 v1, 1
	v_mov_b32_e32 v255, 0
	s_add_u32 s10, s58, 0x2400
	s_addc_u32 s11, s59, 0
	global_atomic_add v255, v1, s[10:11]
	global_atomic_add v255, v1, s[10:11] offset:256
	global_atomic_add v255, v1, s[10:11] offset:512
	global_atomic_add v255, v1, s[10:11] offset:768
	global_atomic_add v255, v1, s[10:11] offset:1024
	global_atomic_add v255, v1, s[10:11] offset:1280
	global_atomic_add v255, v1, s[10:11] offset:1536
	global_atomic_add v255, v1, s[10:11] offset:1792
	global_atomic_add v255, v1, s[10:11] offset:2048
	global_atomic_add v255, v1, s[10:11] offset:2304
	global_atomic_add v255, v1, s[10:11] offset:2560
	global_atomic_add v255, v1, s[10:11] offset:2816
	global_atomic_add v255, v1, s[10:11] offset:3072
	global_atomic_add v255, v1, s[10:11] offset:3328
	global_atomic_add v255, v1, s[10:11] offset:3584
	global_atomic_add v255, v1, s[10:11] offset:3840
	global_atomic_add v[2:3], v1, off
.LBB0_161:
	s_or_b64 exec, exec, s[6:7]
	v_mov_b32_e32 v1, 0x2000
	v_mov_b32_e32 v2, 1
	s_waitcnt vmcnt(0)
	buffer_inv sc1
	s_waitcnt vmcnt(0)

.LBB0_166:
	s_or_b64 exec, exec, s[4:5]
	v_readlane_b32 s4, v245, 24
	v_readlane_b32 s5, v245, 25
	s_waitcnt vmcnt(0)
	buffer_inv sc1
	s_nop 2
	s_waitcnt vmcnt(0)

.LBB0_269:
	s_or_b64 exec, exec, s[4:5]
	s_and_saveexec_b64 s[4:5], s[6:7]
	s_cbranch_execz .LBB0_271
	s_add_u32 s6, s58, 0x2400
	s_addc_u32 s7, s59, 0
	global_atomic_add v195, v203, s[6:7]
	global_atomic_add v195, v203, s[6:7] offset:256
	global_atomic_add v195, v203, s[6:7] offset:512
	global_atomic_add v195, v203, s[6:7] offset:768
	global_atomic_add v195, v203, s[6:7] offset:1024
	global_atomic_add v195, v203, s[6:7] offset:1280
	global_atomic_add v195, v203, s[6:7] offset:1536
	global_atomic_add v195, v203, s[6:7] offset:1792
	global_atomic_add v195, v203, s[6:7] offset:2048
	global_atomic_add v195, v203, s[6:7] offset:2304
	global_atomic_add v195, v203, s[6:7] offset:2560
	global_atomic_add v195, v203, s[6:7] offset:2816
	global_atomic_add v195, v203, s[6:7] offset:3072
	global_atomic_add v195, v203, s[6:7] offset:3328
	global_atomic_add v195, v203, s[6:7] offset:3584
	global_atomic_add v195, v203, s[6:7] offset:3840
	global_atomic_add v[2:3], v203, off

.LBB0_1867:
	s_add_u32 s6, s58, 0x2400
	s_addc_u32 s7, s59, 0
	global_atomic_add v195, v203, s[6:7]
	global_atomic_add v195, v203, s[6:7] offset:256
	global_atomic_add v195, v203, s[6:7] offset:512
	global_atomic_add v195, v203, s[6:7] offset:768
	global_atomic_add v195, v203, s[6:7] offset:1024
	global_atomic_add v195, v203, s[6:7] offset:1280
	global_atomic_add v195, v203, s[6:7] offset:1536
	global_atomic_add v195, v203, s[6:7] offset:1792
	global_atomic_add v195, v203, s[6:7] offset:2048
	global_atomic_add v195, v203, s[6:7] offset:2304
	global_atomic_add v195, v203, s[6:7] offset:2560
	global_atomic_add v195, v203, s[6:7] offset:2816
	global_atomic_add v195, v203, s[6:7] offset:3072
	global_atomic_add v195, v203, s[6:7] offset:3328
	global_atomic_add v195, v203, s[6:7] offset:3584
	global_atomic_add v195, v203, s[6:7] offset:3840
	global_atomic_add v[2:3], v203, off
	s_getpc_b64 s[98:99]

.LBB0_2003:
	s_or_b64 exec, exec, s[2:3]
	s_and_saveexec_b64 s[2:3], s[4:5]
	s_cbranch_execz .LBB0_2005
	v_mov_b32_e32 v2, 1
	v_mov_b32_e32 v255, 0
	s_add_u32 s4, s58, 0x2400
	s_addc_u32 s5, s59, 0
	global_atomic_add v255, v2, s[4:5]
	global_atomic_add v255, v2, s[4:5] offset:256
	global_atomic_add v255, v2, s[4:5] offset:512
	global_atomic_add v255, v2, s[4:5] offset:768
	global_atomic_add v255, v2, s[4:5] offset:1024
	global_atomic_add v255, v2, s[4:5] offset:1280
	global_atomic_add v255, v2, s[4:5] offset:1536
	global_atomic_add v255, v2, s[4:5] offset:1792
	global_atomic_add v255, v2, s[4:5] offset:2048
	global_atomic_add v255, v2, s[4:5] offset:2304
	global_atomic_add v255, v2, s[4:5] offset:2560
	global_atomic_add v255, v2, s[4:5] offset:2816
	global_atomic_add v255, v2, s[4:5] offset:3072
	global_atomic_add v255, v2, s[4:5] offset:3328
	global_atomic_add v255, v2, s[4:5] offset:3584
	global_atomic_add v255, v2, s[4:5] offset:3840
	global_atomic_add v[0:1], v2, off
.LBB0_2005:
	s_or_b64 exec, exec, s[2:3]
	v_readlane_b32 s2, v245, 24
	v_mov_b32_e32 v0, 0
	v_mov_b32_e32 v1, 1
	v_readlane_b32 s3, v245, 25
	s_waitcnt vmcnt(0)
	buffer_inv sc1
	s_nop 2
	s_waitcnt vmcnt(0)
